# ssd_out epilogue: D load at item top, z loads hoisted after last MFMA, 64 in-place LDS updates batched 4x16
# speedup vs baseline: 1.0152x; 1.0078x over previous
.LBB0_641:
	s_and_b32 s21, s91, 0x1ff
	s_lshl_b32 s20, s21, 6
	v_add_u32_e32 v201, s20, v132
	v_lshlrev_b32_e32 v0, 5, v201
	global_load_dword v0, v0, s[18:19]
	s_nop 0
	global_load_dword v1, v209, s[6:7]
	global_load_dword v2, v209, s[8:9]
	s_mov_b32 s12, 0xbfb8aa3b
	v_add_u32_e32 v3, s20, v141
	v_add_u32_e32 v4, s20, v142
	v_add_u32_e32 v5, s20, v143
	v_add_u32_e32 v6, s20, v144
	v_add_u32_e32 v8, s20, v145
	v_add_u32_e32 v10, s20, v146
	v_add_u32_e32 v12, s20, v147
	v_add_u32_e32 v14, s20, v148
	v_add_u32_e32 v16, s20, v149
	v_add_u32_e32 v17, s20, v150
	v_add_u32_e32 v18, s20, v151
	v_add_u32_e32 v19, s20, v152
	s_waitcnt vmcnt(1)
	v_add_f32_e32 v0, v0, v1
	v_mul_f32_e64 v1, |v0|, s12
	v_exp_f32_e32 v7, v1
	s_waitcnt vmcnt(0)
	s_load_dwordx2 s[98:99], s[92:93], 0x80
	s_waitcnt lgkmcnt(0)
	s_add_u32 s98, s98, s4
	s_addc_u32 s99, s99, s5
	global_load_dword v231, v209, s[98:99]
	v_mul_f32_e32 v1, 0x3fb8aa3b, v2
	v_exp_f32_e32 v9, v1
	v_max_f32_e32 v2, 0, v0
	v_add_f32_e32 v11, 1.0, v7
	v_add_f32_e32 v13, -1.0, v11
	v_frexp_mant_f32_e32 v15, v11
	v_cvt_f64_f32_e32 v[0:1], v11
	s_mov_b32 s12, 0x3f2aaaab
	v_sub_f32_e32 v20, v13, v11
	v_frexp_exp_i32_f64_e32 v0, v[0:1]
	v_cmp_gt_f32_e32 vcc, s12, v15
	v_sub_f32_e32 v13, v7, v13
	v_add_f32_e32 v1, 1.0, v20
	v_subbrev_co_u32_e32 v0, vcc, 0, v0, vcc
	v_add_f32_e32 v1, v13, v1
	v_sub_u32_e32 v13, 0, v0
	v_cvt_f32_i32_e32 v0, v0
	v_ldexp_f32 v11, v11, v13
	v_ldexp_f32 v1, v1, v13
	v_add_f32_e32 v13, -1.0, v11
	v_add_f32_e32 v15, 1.0, v11
	v_add_f32_e32 v20, 1.0, v13
	v_add_f32_e32 v21, -1.0, v15
	v_sub_f32_e32 v20, v11, v20
	v_sub_f32_e32 v11, v11, v21
	v_mul_f32_e32 v21, 0x3f317218, v0
	v_add_f32_e32 v20, v1, v20
	v_add_f32_e32 v1, v1, v11
	s_mov_b32 s12, 0x3f317218
	v_fma_f32 v11, v0, s12, -v21
	v_add_f32_e32 v22, v13, v20
	v_add_f32_e32 v23, v15, v1
	v_fmac_f32_e32 v11, 0xb102e308, v0
	v_sub_f32_e32 v0, v22, v13
	v_sub_f32_e32 v13, v23, v15
	v_rcp_f32_e32 v15, v23
	v_add_f32_e32 v24, v21, v11
	v_sub_f32_e32 v1, v1, v13
	v_sub_f32_e32 v13, v24, v21
	v_sub_f32_e32 v11, v11, v13
	v_mul_f32_e32 v13, v22, v15
	v_sub_f32_e32 v0, v20, v0
	v_mul_f32_e32 v20, v23, v13
	v_fma_f32 v21, v13, v23, -v20
	v_fmac_f32_e32 v21, v13, v1
	v_add_f32_e32 v25, v20, v21
	v_sub_f32_e32 v26, v22, v25
	v_sub_f32_e32 v20, v25, v20
	v_sub_f32_e32 v22, v22, v26
	v_sub_f32_e32 v20, v20, v21
	v_sub_f32_e32 v21, v22, v25
	v_add_f32_e32 v0, v0, v21
	v_add_f32_e32 v0, v20, v0
	v_add_f32_e32 v20, v26, v0
	v_mul_f32_e32 v21, v15, v20
	v_sub_f32_e32 v22, v26, v20
	v_mul_f32_e32 v25, v23, v21
	v_add_f32_e32 v0, v0, v22
	v_add_f32_e32 v22, v13, v21
	v_fma_f32 v23, v21, v23, -v25
	v_sub_f32_e32 v13, v22, v13
	v_fmac_f32_e32 v23, v21, v1
	v_sub_f32_e32 v1, v21, v13
	v_add_f32_e32 v13, v25, v23
	v_sub_f32_e32 v21, v13, v25
	v_sub_f32_e32 v25, v20, v13
	v_sub_f32_e32 v20, v20, v25
	v_sub_f32_e32 v13, v20, v13
	v_sub_f32_e32 v21, v21, v23
	v_add_f32_e32 v0, v0, v13
	v_add_f32_e32 v0, v21, v0
	v_add_f32_e32 v0, v25, v0
	v_mul_f32_e32 v0, v15, v0
	v_add_f32_e32 v0, v1, v0
	v_add_f32_e32 v1, v22, v0
	v_mul_f32_e32 v13, v1, v1
	v_fmamk_f32 v21, v13, 0x3e9b6dac, v250
	v_sub_f32_e32 v15, v1, v22
	v_ldexp_f32 v20, v1, 1
	v_mul_f32_e32 v1, v1, v13
	v_fmaak_f32 v13, v13, v21, 0x3f2aaada
	v_mul_f32_e32 v1, v1, v13
	v_add_f32_e32 v13, v20, v1
	v_sub_f32_e32 v0, v0, v15
	v_sub_f32_e32 v15, v13, v20
	v_ldexp_f32 v0, v0, 1
	v_sub_f32_e32 v1, v1, v15
	v_add_f32_e32 v0, v0, v1
	v_add_f32_e32 v1, v13, v0
	v_sub_f32_e32 v13, v1, v13
	v_add_f32_e32 v15, v24, v1
	v_sub_f32_e32 v0, v0, v13
	v_sub_f32_e32 v13, v15, v24
	v_sub_f32_e32 v20, v15, v13
	v_sub_f32_e32 v1, v1, v13
	v_add_f32_e32 v13, v11, v0
	v_sub_f32_e32 v20, v24, v20
	v_sub_f32_e32 v21, v13, v11
	v_add_f32_e32 v1, v1, v20
	v_sub_f32_e32 v20, v13, v21
	v_sub_f32_e32 v0, v0, v21
	v_sub_f32_e32 v11, v11, v20
	v_add_f32_e32 v1, v13, v1
	v_add_f32_e32 v0, v0, v11
	v_add_f32_e32 v11, v15, v1
	v_sub_f32_e32 v13, v11, v15
	v_sub_f32_e32 v1, v1, v13
	v_add_f32_e32 v0, v0, v1
	s_mov_b32 s12, 0x7f800000
	v_add_f32_e32 v0, v11, v0
	v_cmp_neq_f32_e32 vcc, s12, v7
	v_mov_b32_e32 v1, 0x7fc00000
	s_mov_b32 s12, 0x33800000
	v_cndmask_b32_e32 v0, v251, v0, vcc
	v_cmp_ngt_f32_e32 vcc, -1.0, v7
	s_nop 1
	v_cndmask_b32_e32 v0, v1, v0, vcc
	v_cmp_neq_f32_e32 vcc, -1.0, v7
	s_nop 1
	v_cndmask_b32_e32 v0, v230, v0, vcc
	v_cmp_lt_f32_e64 vcc, |v7|, s12
	s_nop 1
	v_cndmask_b32_e32 v0, v0, v7, vcc
	v_add_f32_e32 v20, v2, v0
	v_mul_f32_e64 v7, v20, -v9
	ds_bpermute_b32 v11, v134, v7
	v_mad_i64_i32 v[0:1], s[12:13], v3, s33, v[104:105]
	v_mad_i64_i32 v[2:3], s[12:13], v4, s33, v[106:107]
	v_readlane_b32 s12, v253, 43
	s_waitcnt lgkmcnt(0)
	v_fma_f32 v4, v20, -v9, v11
	v_readlane_b32 s13, v253, 44
	s_nop 1
	v_cndmask_b32_e64 v9, v4, v7, s[12:13]
	ds_bpermute_b32 v11, v135, v9
	v_mad_i64_i32 v[4:5], s[12:13], v5, s33, v[108:109]
	v_mad_i64_i32 v[6:7], s[12:13], v6, s33, v[110:111]
	v_readlane_b32 s12, v253, 47
	s_waitcnt lgkmcnt(0)
	v_add_f32_e32 v11, v9, v11
	v_readlane_b32 s13, v253, 48
	s_nop 1
	v_cndmask_b32_e64 v13, v11, v9, s[12:13]
	ds_bpermute_b32 v15, v136, v13
	v_mad_i64_i32 v[8:9], s[12:13], v8, s33, v[112:113]
	v_mad_i64_i32 v[10:11], s[12:13], v10, s33, v[114:115]
	v_readlane_b32 s12, v253, 49
	s_waitcnt lgkmcnt(0)
	v_add_f32_e32 v15, v13, v15
	v_readlane_b32 s13, v253, 50
	s_nop 1
	v_cndmask_b32_e64 v21, v15, v13, s[12:13]
	ds_bpermute_b32 v22, v137, v21
	v_mad_i64_i32 v[12:13], s[12:13], v12, s33, v[116:117]
	v_mad_i64_i32 v[14:15], s[12:13], v14, s33, v[118:119]
	v_readlane_b32 s12, v253, 45
	s_waitcnt lgkmcnt(0)
	v_add_f32_e32 v22, v21, v22
	v_readlane_b32 s13, v253, 46
	s_nop 1
	v_cndmask_b32_e64 v21, v22, v21, s[12:13]
	ds_bpermute_b32 v22, v138, v21
	v_mad_i64_i32 v[48:49], s[12:13], v16, s33, v[120:121]
	v_mad_i64_i32 v[50:51], s[12:13], v17, s33, v[122:123]
	v_readlane_b32 s12, v253, 51
	s_waitcnt lgkmcnt(0)
	v_add_f32_e32 v16, v21, v22
	v_readlane_b32 s13, v253, 52
	s_nop 1
	v_cndmask_b32_e64 v16, v16, v21, s[12:13]
	ds_bpermute_b32 v17, v139, v16
	v_mad_i64_i32 v[52:53], s[12:13], v18, s33, v[124:125]
	v_mad_i64_i32 v[54:55], s[12:13], v19, s33, v[126:127]
	v_readlane_b32 s12, v253, 55
	s_waitcnt lgkmcnt(0)
	v_add_f32_e32 v17, v16, v17
	v_readlane_b32 s13, v253, 56
	s_nop 1
	v_cndmask_b32_e64 v16, v17, v16, s[12:13]
	ds_write2st64_b32 v140, v16, v20 offset1:8
	s_waitcnt lgkmcnt(0)
	s_barrier
	global_load_dwordx4 v[44:47], v[0:1], off
	global_load_dwordx4 v[40:43], v[2:3], off
	global_load_dwordx4 v[36:39], v[4:5], off
	global_load_dwordx4 v[32:35], v[6:7], off
	global_load_dwordx4 v[28:31], v[8:9], off
	global_load_dwordx4 v[24:27], v[10:11], off
	global_load_dwordx4 v[20:23], v[12:13], off
	global_load_dwordx4 v[16:19], v[14:15], off
	s_nop 0
	global_load_dwordx4 v[12:15], v[48:49], off
	global_load_dwordx4 v[8:11], v[50:51], off
	global_load_dwordx4 v[4:7], v[52:53], off
	global_load_dwordx4 v[0:3], v[54:55], off
	s_mov_b64 s[12:13], exec
	v_readlane_b32 s76, v253, 59
	v_readlane_b32 s77, v253, 60
	s_and_b64 s[76:77], s[12:13], s[76:77]
	s_xor_b64 vcc, s[76:77], s[12:13]
	s_mov_b64 exec, s[76:77]
	s_cbranch_execz .LBB0_647
	s_mov_b64 s[12:13], exec
	v_readlane_b32 s76, v253, 61
	v_readlane_b32 s77, v253, 62
	s_and_b64 s[76:77], s[12:13], s[76:77]
	s_xor_b64 s[12:13], s[76:77], s[12:13]
	s_mov_b64 exec, s[76:77]
	s_cbranch_execz .LBB0_644
	s_waitcnt vmcnt(11)
	ds_write_b128 v157, v[44:47] offset:22528

.LBB0_833:
	s_or_b64 exec, exec, vcc
	s_lshl_b32 s12, s21, 3
	s_add_i32 s12, s12, s90
	s_ashr_i32 s13, s12, 31
	s_lshl_b64 s[12:13], s[12:13], 13
	v_cvt_pk_bf16_f32 v88, v50, v49
	v_lshl_add_u64 v[50:51], v[128:129], 0, s[12:13]
	v_mov_b32_e32 v131, v209
	v_cvt_pk_bf16_f32 v92, v16, v17
	v_cvt_pk_bf16_f32 v100, v0, v1
	v_cvt_pk_bf16_f32 v89, v33, v32
	v_mov_b32_e32 v32, v209
	v_mov_b32_e32 v64, v209
	v_mov_b32_e32 v0, v209
	v_mov_b32_e32 v16, v209
	s_waitcnt lgkmcnt(0)
	v_lshl_add_u64 v[48:49], v[50:51], 0, v[208:209]
	v_lshl_add_u64 v[50:51], v[50:51], 0, v[130:131]
	global_load_dwordx4 v[52:55], v[48:49], off
	global_load_dwordx4 v[56:59], v[50:51], off
	global_load_dwordx4 v[226:229], v[48:49], off offset:32
	global_load_dwordx4 v[232:235], v[50:51], off offset:32
	global_load_dwordx4 v[236:239], v[48:49], off offset:64
	global_load_dwordx4 v[240:243], v[50:51], off offset:64
	global_load_dwordx4 v[244:247], v[48:49], off offset:96
	s_nop 0
	global_load_dwordx4 v[48:51], v[50:51], off offset:96
	ds_read_b128 v[60:63], v193 offset:22528
	ds_read_b128 v[202:205], v193 offset:22560
	v_cvt_pk_bf16_f32 v90, v35, v34
	v_cvt_pk_bf16_f32 v91, v37, v36
	v_cvt_pk_bf16_f32 v80, v39, v38
	v_cvt_pk_bf16_f32 v81, v41, v40
	v_cvt_pk_bf16_f32 v82, v43, v42
	v_cvt_pk_bf16_f32 v83, v45, v44
	v_mov_b32_e32 v33, v32
	v_mov_b32_e32 v34, v32
	v_mov_b32_e32 v35, v32
	v_mov_b32_e32 v36, v32
	v_mov_b32_e32 v37, v32
	v_mov_b32_e32 v38, v32
	v_mov_b32_e32 v39, v32
	v_mov_b32_e32 v40, v32
	v_mov_b32_e32 v41, v32
	v_mov_b32_e32 v42, v32
	v_mov_b32_e32 v43, v32
	v_mov_b32_e32 v44, v32
	v_mov_b32_e32 v45, v32
	v_mov_b32_e32 v46, v32
	v_mov_b32_e32 v47, v32
	v_mov_b32_e32 v65, v64
	v_mov_b32_e32 v66, v64
	v_mov_b32_e32 v67, v64
	v_mov_b32_e32 v68, v64
	v_mov_b32_e32 v69, v64
	v_mov_b32_e32 v70, v64
	v_mov_b32_e32 v71, v64
	v_mov_b32_e32 v72, v64
	v_mov_b32_e32 v73, v64
	v_mov_b32_e32 v74, v64
	v_mov_b32_e32 v75, v64
	v_mov_b32_e32 v76, v64
	v_mov_b32_e32 v77, v64
	v_mov_b32_e32 v78, v64
	v_mov_b32_e32 v79, v64
	v_cvt_pk_bf16_f32 v93, v18, v19
	v_cvt_pk_bf16_f32 v94, v20, v21
	v_cvt_pk_bf16_f32 v95, v22, v23
	v_cvt_pk_bf16_f32 v84, v24, v25
	v_cvt_pk_bf16_f32 v85, v26, v27
	v_cvt_pk_bf16_f32 v86, v28, v29
	v_cvt_pk_bf16_f32 v87, v30, v31
	v_cvt_pk_bf16_f32 v101, v2, v3
	v_cvt_pk_bf16_f32 v102, v4, v5
	v_cvt_pk_bf16_f32 v103, v6, v7
	v_cvt_pk_bf16_f32 v96, v8, v9
	v_cvt_pk_bf16_f32 v97, v10, v11
	v_cvt_pk_bf16_f32 v98, v12, v13
	v_cvt_pk_bf16_f32 v99, v14, v15
	v_mov_b32_e32 v1, v0
	v_mov_b32_e32 v2, v0
	v_mov_b32_e32 v3, v0
	v_mov_b32_e32 v4, v0
	v_mov_b32_e32 v5, v0
	v_mov_b32_e32 v6, v0
	v_mov_b32_e32 v7, v0
	v_mov_b32_e32 v8, v0
	v_mov_b32_e32 v9, v0
	v_mov_b32_e32 v10, v0
	v_mov_b32_e32 v11, v0
	v_mov_b32_e32 v12, v0
	v_mov_b32_e32 v13, v0
	s_waitcnt vmcnt(7) lgkmcnt(1)
	v_mfma_f32_32x32x16_bf16 v[32:47], v[60:63], v[52:55], v[32:47]
	v_mov_b32_e32 v14, v0
	v_mov_b32_e32 v15, v0
	v_mov_b32_e32 v17, v16
	v_mov_b32_e32 v18, v16
	v_mov_b32_e32 v19, v16
	v_mov_b32_e32 v20, v16
	v_mov_b32_e32 v21, v16
	s_waitcnt vmcnt(6)
	v_mfma_f32_32x32x16_bf16 v[64:79], v[60:63], v[56:59], v[64:79]
	ds_read_b128 v[60:63], v194 offset:22528
	ds_read_b128 v[210:213], v194 offset:22560
	v_mov_b32_e32 v22, v16
	v_mov_b32_e32 v23, v16
	v_mov_b32_e32 v24, v16
	v_mov_b32_e32 v25, v16
	v_mov_b32_e32 v26, v16
	v_mov_b32_e32 v27, v16
	v_mov_b32_e32 v28, v16
	v_mov_b32_e32 v29, v16
	v_mov_b32_e32 v30, v16
	v_mov_b32_e32 v31, v16
	s_waitcnt lgkmcnt(1)
	v_mfma_f32_32x32x16_bf16 v[0:15], v[60:63], v[52:55], v[0:15]
	v_mfma_f32_32x32x16_bf16 v[16:31], v[60:63], v[56:59], v[16:31]
	ds_read_b128 v[60:63], v194 offset:22592
	s_waitcnt vmcnt(5)
	v_mfma_f32_32x32x16_bf16 v[32:47], v[202:205], v[226:229], v[32:47]
	s_waitcnt vmcnt(4)
	v_mfma_f32_32x32x16_bf16 v[64:79], v[202:205], v[232:235], v[64:79]
	s_waitcnt lgkmcnt(1)
	v_mfma_f32_32x32x16_bf16 v[16:31], v[210:213], v[232:235], v[16:31]
	v_mfma_f32_32x32x16_bf16 v[0:15], v[210:213], v[226:229], v[0:15]
	ds_read_b128 v[52:55], v193 offset:22592
	s_waitcnt vmcnt(3) lgkmcnt(0)
	v_mfma_f32_32x32x16_bf16 v[32:47], v[52:55], v[236:239], v[32:47]
	v_mfma_f32_32x32x16_bf16 v[0:15], v[60:63], v[236:239], v[0:15]
	s_waitcnt vmcnt(2)
	v_mfma_f32_32x32x16_bf16 v[64:79], v[52:55], v[240:243], v[64:79]
	ds_read_b128 v[52:55], v193 offset:22624
	v_mfma_f32_32x32x16_bf16 v[16:31], v[60:63], v[240:243], v[16:31]
	ds_read_b128 v[60:63], v194 offset:22624
	s_waitcnt vmcnt(1) lgkmcnt(1)
	v_mfma_f32_32x32x16_bf16 v[32:47], v[52:55], v[244:247], v[32:47]
	s_waitcnt vmcnt(0)
	v_mfma_f32_32x32x16_bf16 v[64:79], v[52:55], v[48:51], v[64:79]
	s_waitcnt lgkmcnt(0)
	v_mfma_f32_32x32x16_bf16 v[16:31], v[60:63], v[48:51], v[16:31]
	ds_read_b128 v[48:51], v154
	ds_read_b128 v[52:55], v154 offset:32
	s_waitcnt lgkmcnt(1)
	v_mul_f32_e32 v48, 0x3fb8aa3b, v48
	v_exp_f32_e32 v202, v48
	v_mul_f32_e32 v48, 0x3fb8aa3b, v49
	v_exp_f32_e32 v203, v48
	v_mul_f32_e32 v48, 0x3fb8aa3b, v50
	v_exp_f32_e32 v204, v48
	v_mul_f32_e32 v48, 0x3fb8aa3b, v51
	v_exp_f32_e32 v205, v48
	s_waitcnt lgkmcnt(0)
	v_mul_f32_e32 v48, 0x3fb8aa3b, v52
	v_exp_f32_e32 v206, v48
	v_mul_f32_e32 v48, 0x3fb8aa3b, v53
	v_exp_f32_e32 v207, v48
	v_mul_f32_e32 v48, 0x3fb8aa3b, v54
	v_exp_f32_e32 v210, v48
	v_mul_f32_e32 v48, 0x3fb8aa3b, v55
	v_exp_f32_e32 v211, v48
	ds_read_b128 v[48:51], v154 offset:64
	v_pk_mul_f32 v[52:53], v[36:37], v[206:207]
	v_pk_mul_f32 v[36:37], v[68:69], v[206:207]
	v_pk_mul_f32 v[54:55], v[38:39], v[210:211]
	v_pk_mul_f32 v[38:39], v[70:71], v[210:211]
	s_waitcnt lgkmcnt(0)
	v_mul_f32_e32 v48, 0x3fb8aa3b, v48
	v_exp_f32_e32 v212, v48
	v_mul_f32_e32 v48, 0x3fb8aa3b, v49
	v_exp_f32_e32 v213, v48
	v_mul_f32_e32 v48, 0x3fb8aa3b, v50
	v_exp_f32_e32 v214, v48
	v_mul_f32_e32 v48, 0x3fb8aa3b, v51
	v_exp_f32_e32 v215, v48
	ds_read_b128 v[48:51], v154 offset:96
	v_mfma_f32_32x32x16_bf16 v[0:15], v[60:63], v[244:247], v[0:15]
	v_mul_f32_e64 v56, v40, v212
	v_mul_f32_e64 v57, v41, v213
	v_mul_f32_e64 v40, v72, v212
	v_mul_f32_e64 v41, v73, v213
	v_mul_f32_e64 v58, v42, v214
	v_mul_f32_e64 v59, v43, v215
	s_waitcnt lgkmcnt(0)
	v_mul_f32_e32 v48, 0x3fb8aa3b, v48
	v_exp_f32_e32 v216, v48
	v_mul_f32_e32 v48, 0x3fb8aa3b, v49
	v_exp_f32_e32 v217, v48
	v_mul_f32_e32 v48, 0x3fb8aa3b, v50
	v_exp_f32_e32 v218, v48
	v_mul_f32_e32 v48, 0x3fb8aa3b, v51
	v_exp_f32_e32 v219, v48
	v_pk_mul_f32 v[50:51], v[34:35], v[204:205]
	v_pk_mul_f32 v[48:49], v[32:33], v[202:203]
	v_pk_mul_f32 v[34:35], v[66:67], v[204:205]
	v_pk_mul_f32 v[32:33], v[64:65], v[202:203]
	ds_read_b128 v[64:67], v154 offset:128
	v_pk_mul_f32 v[42:43], v[74:75], v[214:215]
	v_pk_mul_f32 v[60:61], v[44:45], v[216:217]
	v_pk_mul_f32 v[44:45], v[76:77], v[216:217]
	v_pk_mul_f32 v[62:63], v[46:47], v[218:219]
	s_waitcnt lgkmcnt(0)
	v_mul_f32_e32 v64, 0x3fb8aa3b, v64
	v_exp_f32_e32 v68, v64
	v_mul_f32_e32 v64, 0x3fb8aa3b, v65
	v_exp_f32_e32 v69, v64
	v_mul_f32_e32 v64, 0x3fb8aa3b, v66
	v_exp_f32_e32 v70, v64
	v_mul_f32_e32 v64, 0x3fb8aa3b, v67
	v_exp_f32_e32 v71, v64
	ds_read_b128 v[64:67], v154 offset:160
	v_pk_mul_f32 v[46:47], v[78:79], v[218:219]
	v_pk_mul_f32 v[0:1], v[0:1], v[68:69]
	v_pk_mul_f32 v[2:3], v[2:3], v[70:71]
	v_pk_mul_f32 v[18:19], v[18:19], v[70:71]
	s_waitcnt lgkmcnt(0)
	v_mul_f32_e32 v64, 0x3fb8aa3b, v64
	v_exp_f32_e32 v72, v64
	v_mul_f32_e32 v64, 0x3fb8aa3b, v65
	v_exp_f32_e32 v73, v64
	v_mul_f32_e32 v64, 0x3fb8aa3b, v66
	v_exp_f32_e32 v74, v64
	v_mul_f32_e32 v64, 0x3fb8aa3b, v67
	v_exp_f32_e32 v75, v64
	ds_read_b128 v[64:67], v154 offset:192
	v_pk_mul_f32 v[4:5], v[4:5], v[72:73]
	v_pk_mul_f32 v[16:17], v[16:17], v[68:69]
	v_pk_mul_f32 v[6:7], v[6:7], v[74:75]
	v_pk_mul_f32 v[22:23], v[22:23], v[74:75]
	s_waitcnt lgkmcnt(0)
	v_mul_f32_e32 v64, 0x3fb8aa3b, v64
	v_exp_f32_e32 v76, v64
	v_mul_f32_e32 v64, 0x3fb8aa3b, v65
	v_exp_f32_e32 v77, v64
	v_mul_f32_e32 v64, 0x3fb8aa3b, v66
	v_exp_f32_e32 v78, v64
	v_mul_f32_e32 v64, 0x3fb8aa3b, v67
	v_exp_f32_e32 v79, v64
	ds_read_b128 v[64:67], v154 offset:224
	v_pk_mul_f32 v[8:9], v[8:9], v[76:77]
	v_pk_mul_f32 v[20:21], v[20:21], v[72:73]
	v_pk_mul_f32 v[10:11], v[10:11], v[78:79]
	v_pk_mul_f32 v[26:27], v[26:27], v[78:79]
	s_waitcnt lgkmcnt(0)
	v_mul_f32_e32 v64, 0x3fb8aa3b, v64
	v_mul_f32_e32 v65, 0x3fb8aa3b, v65
	v_mul_f32_e32 v66, 0x3fb8aa3b, v66
	v_mul_f32_e32 v67, 0x3fb8aa3b, v67
	v_exp_f32_e32 v64, v64
	v_exp_f32_e32 v65, v65
	v_exp_f32_e32 v66, v66
	v_exp_f32_e32 v67, v67
	v_pk_mul_f32 v[24:25], v[24:25], v[76:77]
	v_pk_mul_f32 v[12:13], v[12:13], v[64:65]
	v_pk_mul_f32 v[28:29], v[28:29], v[64:65]
	v_pk_mul_f32 v[14:15], v[14:15], v[66:67]
	v_pk_mul_f32 v[30:31], v[30:31], v[66:67]
	ds_read_b64_tr_b16 v[64:65], v195 offset:40960
	ds_read_b64_tr_b16 v[66:67], v195 offset:41984
	ds_read_b64_tr_b16 v[68:69], v196 offset:40960
	ds_read_b64_tr_b16 v[70:71], v196 offset:41984
	s_waitcnt lgkmcnt(2)
	v_mfma_f32_32x32x16_bf16 v[0:15], v[92:95], v[64:67], v[0:15]
	ds_read_b64_tr_b16 v[72:73], v195 offset:43008
	ds_read_b64_tr_b16 v[74:75], v195 offset:44032
	ds_read_b64_tr_b16 v[76:77], v196 offset:43008
	ds_read_b64_tr_b16 v[78:79], v196 offset:44032
	s_waitcnt lgkmcnt(4)
	v_mfma_f32_32x32x16_bf16 v[16:31], v[92:95], v[68:71], v[16:31]
	s_waitcnt lgkmcnt(2)
	v_mfma_f32_32x32x16_bf16 v[0:15], v[84:87], v[72:75], v[0:15]
	v_mfma_f32_32x32x16_bf16 v[48:63], v[100:103], v[64:67], v[48:63]
	ds_read_b64_tr_b16 v[64:65], v195 offset:45056
	ds_read_b64_tr_b16 v[66:67], v195 offset:46080
	s_waitcnt lgkmcnt(2)
	v_mfma_f32_32x32x16_bf16 v[16:31], v[84:87], v[76:79], v[16:31]
	s_waitcnt lgkmcnt(0)
	v_mfma_f32_32x32x16_bf16 v[0:15], v[88:91], v[64:67], v[0:15]
	ds_read_b64_tr_b16 v[64:65], v196 offset:45056
	ds_read_b64_tr_b16 v[66:67], v196 offset:46080
	s_waitcnt lgkmcnt(0)
	v_mfma_f32_32x32x16_bf16 v[16:31], v[88:91], v[64:67], v[16:31]
	ds_read_b64_tr_b16 v[64:65], v195 offset:47104
	ds_read_b64_tr_b16 v[66:67], v195 offset:48128
	s_waitcnt lgkmcnt(0)
	v_mfma_f32_32x32x16_bf16 v[0:15], v[80:83], v[64:67], v[0:15]
	ds_read_b64_tr_b16 v[64:65], v196 offset:47104
	ds_read_b64_tr_b16 v[66:67], v196 offset:48128
	s_waitcnt lgkmcnt(0)
	v_mfma_f32_32x32x16_bf16 v[16:31], v[80:83], v[64:67], v[16:31]
	v_mfma_f32_32x32x16_bf16 v[48:63], v[96:99], v[72:75], v[48:63]
	v_mfma_f32_32x32x16_bf16 v[32:47], v[100:103], v[68:71], v[32:47]
	v_mfma_f32_32x32x16_bf16 v[32:47], v[96:99], v[76:79], v[32:47]
	s_waitcnt vmcnt(0)
	v_mov_b64_e32 v[202:203], s[10:11]
	v_mad_u64_u32 v[202:203], s[98:99], v201, s62, v[202:203]
	v_lshl_add_u64 v[204:205], s[94:95], 1, v[202:203]
	v_mov_b32_e32 v202, s82
	v_mov_b32_e32 v203, 0
	s_mov_b64 s[98:99], 0x1000
	v_lshl_add_u64 v[202:203], v[204:205], 0, v[202:203]
	v_lshl_add_u64 v[204:205], v[204:205], 0, s[98:99]
	global_load_dwordx4 v[210:213], v[202:203], off
	global_load_dwordx4 v[214:217], v[204:205], off offset:48
	global_load_dwordx4 v[218:221], v[204:205], off offset:32
	global_load_dwordx4 v[226:229], v[204:205], off offset:16
	global_load_dwordx4 v[232:235], v[204:205], off offset:112
	global_load_dwordx4 v[236:239], v[204:205], off offset:96
	global_load_dwordx4 v[240:243], v[204:205], off offset:80
	global_load_dwordx4 v[244:247], v[204:205], off offset:64
	ds_read_u16 v80, v155 offset:40960
	ds_read_u16 v81, v155 offset:41024
	ds_read_u16 v82, v155 offset:41088
	ds_read_u16 v83, v155 offset:41152
	ds_read_u16 v84, v155 offset:41280
	ds_read_u16 v85, v155 offset:41216
	ds_read_u16 v86, v155 offset:41408
	ds_read_u16 v87, v155 offset:41344
	ds_read_u16 v88, v155 offset:41984
	ds_read_u16 v89, v155 offset:42048
	ds_read_u16 v90, v155 offset:42112
	ds_read_u16 v91, v155 offset:42176
	ds_read_u16 v92, v155 offset:42304
	ds_read_u16 v93, v155 offset:42240
	ds_read_u16 v94, v155 offset:42432
	ds_read_u16 v95, v155 offset:42368
	s_nop 7
	s_nop 7
	s_waitcnt lgkmcnt(15)
	v_lshlrev_b32_e32 v80, 16, v80
	v_fma_f32 v80, v231, v80, v48
	v_bfe_u32 v206, v80, 16, 1
	v_add3_u32 v80, v80, v206, s63
	ds_write_b16_d16_hi v155, v80 offset:40960
	s_waitcnt lgkmcnt(15)
	v_lshlrev_b32_e32 v81, 16, v81
	v_fma_f32 v81, v231, v81, v32
	v_bfe_u32 v206, v81, 16, 1
	v_add3_u32 v81, v81, v206, s63
	ds_write_b16_d16_hi v155, v81 offset:41024
	s_waitcnt lgkmcnt(15)
	v_lshlrev_b32_e32 v82, 16, v82
	v_fma_f32 v82, v231, v82, v49
	v_bfe_u32 v206, v82, 16, 1
	v_add3_u32 v82, v82, v206, s63
	ds_write_b16_d16_hi v155, v82 offset:41088
	s_waitcnt lgkmcnt(15)
	v_lshlrev_b32_e32 v83, 16, v83
	v_fma_f32 v83, v231, v83, v33
	v_bfe_u32 v206, v83, 16, 1
	v_add3_u32 v83, v83, v206, s63
	ds_write_b16_d16_hi v155, v83 offset:41152
	s_waitcnt lgkmcnt(15)
	v_lshlrev_b32_e32 v84, 16, v84
	v_fma_f32 v84, v231, v84, v50
	v_bfe_u32 v206, v84, 16, 1
	v_add3_u32 v84, v84, v206, s63
	ds_write_b16_d16_hi v155, v84 offset:41280
	s_waitcnt lgkmcnt(15)
	v_lshlrev_b32_e32 v85, 16, v85
	v_fma_f32 v85, v231, v85, v34
	v_bfe_u32 v206, v85, 16, 1
	v_add3_u32 v85, v85, v206, s63
	ds_write_b16_d16_hi v155, v85 offset:41216
	s_waitcnt lgkmcnt(15)
	v_lshlrev_b32_e32 v86, 16, v86
	v_fma_f32 v86, v231, v86, v51
	v_bfe_u32 v206, v86, 16, 1
	v_add3_u32 v86, v86, v206, s63
	ds_write_b16_d16_hi v155, v86 offset:41408
	s_waitcnt lgkmcnt(15)
	v_lshlrev_b32_e32 v87, 16, v87
	v_fma_f32 v87, v231, v87, v35
	v_bfe_u32 v206, v87, 16, 1
	v_add3_u32 v87, v87, v206, s63
	ds_write_b16_d16_hi v155, v87 offset:41344
	s_waitcnt lgkmcnt(15)
	v_lshlrev_b32_e32 v88, 16, v88
	v_fma_f32 v88, v231, v88, v52
	v_bfe_u32 v206, v88, 16, 1
	v_add3_u32 v88, v88, v206, s63
	ds_write_b16_d16_hi v155, v88 offset:41984
	s_waitcnt lgkmcnt(15)
	v_lshlrev_b32_e32 v89, 16, v89
	v_fma_f32 v89, v231, v89, v36
	v_bfe_u32 v206, v89, 16, 1
	v_add3_u32 v89, v89, v206, s63
	ds_write_b16_d16_hi v155, v89 offset:42048
	s_waitcnt lgkmcnt(15)
	v_lshlrev_b32_e32 v90, 16, v90
	v_fma_f32 v90, v231, v90, v53
	v_bfe_u32 v206, v90, 16, 1
	v_add3_u32 v90, v90, v206, s63
	ds_write_b16_d16_hi v155, v90 offset:42112
	s_waitcnt lgkmcnt(15)
	v_lshlrev_b32_e32 v91, 16, v91
	v_fma_f32 v91, v231, v91, v37
	v_bfe_u32 v206, v91, 16, 1
	v_add3_u32 v91, v91, v206, s63
	ds_write_b16_d16_hi v155, v91 offset:42176
	s_waitcnt lgkmcnt(15)
	v_lshlrev_b32_e32 v92, 16, v92
	v_fma_f32 v92, v231, v92, v54
	v_bfe_u32 v206, v92, 16, 1
	v_add3_u32 v92, v92, v206, s63
	ds_write_b16_d16_hi v155, v92 offset:42304
	s_waitcnt lgkmcnt(15)
	v_lshlrev_b32_e32 v93, 16, v93
	v_fma_f32 v93, v231, v93, v38
	v_bfe_u32 v206, v93, 16, 1
	v_add3_u32 v93, v93, v206, s63
	ds_write_b16_d16_hi v155, v93 offset:42240
	s_waitcnt lgkmcnt(15)
	v_lshlrev_b32_e32 v94, 16, v94
	v_fma_f32 v94, v231, v94, v55
	v_bfe_u32 v206, v94, 16, 1
	v_add3_u32 v94, v94, v206, s63
	ds_write_b16_d16_hi v155, v94 offset:42432
	s_waitcnt lgkmcnt(15)
	v_lshlrev_b32_e32 v95, 16, v95
	v_fma_f32 v95, v231, v95, v39
	v_bfe_u32 v206, v95, 16, 1
	v_add3_u32 v95, v95, v206, s63
	ds_write_b16_d16_hi v155, v95 offset:42368
	ds_read_u16 v80, v155 offset:43008
	ds_read_u16 v81, v155 offset:43072
	ds_read_u16 v82, v155 offset:43136
	ds_read_u16 v83, v155 offset:43200
	ds_read_u16 v84, v155 offset:43328
	ds_read_u16 v85, v155 offset:43264
	ds_read_u16 v86, v155 offset:43456
	ds_read_u16 v87, v155 offset:43392
	ds_read_u16 v88, v155 offset:44032
	ds_read_u16 v89, v155 offset:44096
	ds_read_u16 v90, v155 offset:44160
	ds_read_u16 v91, v155 offset:44224
	ds_read_u16 v92, v155 offset:44352
	ds_read_u16 v93, v155 offset:44288
	ds_read_u16 v94, v155 offset:44480
	ds_read_u16 v95, v155 offset:44416
	s_waitcnt lgkmcnt(15)
	v_lshlrev_b32_e32 v80, 16, v80
	v_fma_f32 v80, v231, v80, v56
	v_bfe_u32 v206, v80, 16, 1
	v_add3_u32 v80, v80, v206, s63
	ds_write_b16_d16_hi v155, v80 offset:43008
	s_waitcnt lgkmcnt(15)
	v_lshlrev_b32_e32 v81, 16, v81
	v_fma_f32 v81, v231, v81, v40
	v_bfe_u32 v206, v81, 16, 1
	v_add3_u32 v81, v81, v206, s63
	ds_write_b16_d16_hi v155, v81 offset:43072
	s_waitcnt lgkmcnt(15)
	v_lshlrev_b32_e32 v82, 16, v82
	v_fma_f32 v82, v231, v82, v57
	v_bfe_u32 v206, v82, 16, 1
	v_add3_u32 v82, v82, v206, s63
	ds_write_b16_d16_hi v155, v82 offset:43136
	s_waitcnt lgkmcnt(15)
	v_lshlrev_b32_e32 v83, 16, v83
	v_fma_f32 v83, v231, v83, v41
	v_bfe_u32 v206, v83, 16, 1
	v_add3_u32 v83, v83, v206, s63
	ds_write_b16_d16_hi v155, v83 offset:43200
	s_waitcnt lgkmcnt(15)
	v_lshlrev_b32_e32 v84, 16, v84
	v_fma_f32 v84, v231, v84, v58
	v_bfe_u32 v206, v84, 16, 1
	v_add3_u32 v84, v84, v206, s63
	ds_write_b16_d16_hi v155, v84 offset:43328
	s_waitcnt lgkmcnt(15)
	v_lshlrev_b32_e32 v85, 16, v85
	v_fma_f32 v85, v231, v85, v42
	v_bfe_u32 v206, v85, 16, 1
	v_add3_u32 v85, v85, v206, s63
	ds_write_b16_d16_hi v155, v85 offset:43264
	s_waitcnt lgkmcnt(15)
	v_lshlrev_b32_e32 v86, 16, v86
	v_fma_f32 v86, v231, v86, v59
	v_bfe_u32 v206, v86, 16, 1
	v_add3_u32 v86, v86, v206, s63
	ds_write_b16_d16_hi v155, v86 offset:43456
	s_waitcnt lgkmcnt(15)
	v_lshlrev_b32_e32 v87, 16, v87
	v_fma_f32 v87, v231, v87, v43
	v_bfe_u32 v206, v87, 16, 1
	v_add3_u32 v87, v87, v206, s63
	ds_write_b16_d16_hi v155, v87 offset:43392
	s_waitcnt lgkmcnt(15)
	v_lshlrev_b32_e32 v88, 16, v88
	v_fma_f32 v88, v231, v88, v60
	v_bfe_u32 v206, v88, 16, 1
	v_add3_u32 v88, v88, v206, s63
	ds_write_b16_d16_hi v155, v88 offset:44032
	s_waitcnt lgkmcnt(15)
	v_lshlrev_b32_e32 v89, 16, v89
	v_fma_f32 v89, v231, v89, v44
	v_bfe_u32 v206, v89, 16, 1
	v_add3_u32 v89, v89, v206, s63
	ds_write_b16_d16_hi v155, v89 offset:44096
	s_waitcnt lgkmcnt(15)
	v_lshlrev_b32_e32 v90, 16, v90
	v_fma_f32 v90, v231, v90, v61
	v_bfe_u32 v206, v90, 16, 1
	v_add3_u32 v90, v90, v206, s63
	ds_write_b16_d16_hi v155, v90 offset:44160
	s_waitcnt lgkmcnt(15)
	v_lshlrev_b32_e32 v91, 16, v91
	v_fma_f32 v91, v231, v91, v45
	v_bfe_u32 v206, v91, 16, 1
	v_add3_u32 v91, v91, v206, s63
	ds_write_b16_d16_hi v155, v91 offset:44224
	s_waitcnt lgkmcnt(15)
	v_lshlrev_b32_e32 v92, 16, v92
	v_fma_f32 v92, v231, v92, v62
	v_bfe_u32 v206, v92, 16, 1
	v_add3_u32 v92, v92, v206, s63
	ds_write_b16_d16_hi v155, v92 offset:44352
	s_waitcnt lgkmcnt(15)
	v_lshlrev_b32_e32 v93, 16, v93
	v_fma_f32 v93, v231, v93, v46
	v_bfe_u32 v206, v93, 16, 1
	v_add3_u32 v93, v93, v206, s63
	ds_write_b16_d16_hi v155, v93 offset:44288
	s_waitcnt lgkmcnt(15)
	v_lshlrev_b32_e32 v94, 16, v94
	v_fma_f32 v94, v231, v94, v63
	v_bfe_u32 v206, v94, 16, 1
	v_add3_u32 v94, v94, v206, s63
	ds_write_b16_d16_hi v155, v94 offset:44480
	s_waitcnt lgkmcnt(15)
	v_lshlrev_b32_e32 v95, 16, v95
	v_fma_f32 v95, v231, v95, v47
	v_bfe_u32 v206, v95, 16, 1
	v_add3_u32 v95, v95, v206, s63
	ds_write_b16_d16_hi v155, v95 offset:44416
	ds_read_u16 v80, v155 offset:45056
	ds_read_u16 v81, v155 offset:45120
	ds_read_u16 v82, v155 offset:45184
	ds_read_u16 v83, v155 offset:45248
	ds_read_u16 v84, v155 offset:45376
	ds_read_u16 v85, v155 offset:45312
	ds_read_u16 v86, v155 offset:45504
	ds_read_u16 v87, v155 offset:45440
	ds_read_u16 v88, v155 offset:46080
	ds_read_u16 v89, v155 offset:46144
	ds_read_u16 v90, v155 offset:46208
	ds_read_u16 v91, v155 offset:46272
	ds_read_u16 v92, v155 offset:46400
	ds_read_u16 v93, v155 offset:46336
	ds_read_u16 v94, v155 offset:46528
	ds_read_u16 v95, v155 offset:46464
	s_waitcnt lgkmcnt(15)
	v_lshlrev_b32_e32 v80, 16, v80
	v_fma_f32 v80, v231, v80, v0
	v_bfe_u32 v206, v80, 16, 1
	v_add3_u32 v80, v80, v206, s63
	ds_write_b16_d16_hi v155, v80 offset:45056
	s_waitcnt lgkmcnt(15)
	v_lshlrev_b32_e32 v81, 16, v81
	v_fma_f32 v81, v231, v81, v16
	v_bfe_u32 v206, v81, 16, 1
	v_add3_u32 v81, v81, v206, s63
	ds_write_b16_d16_hi v155, v81 offset:45120
	s_waitcnt lgkmcnt(15)
	v_lshlrev_b32_e32 v82, 16, v82
	v_fma_f32 v82, v231, v82, v1
	v_bfe_u32 v206, v82, 16, 1
	v_add3_u32 v82, v82, v206, s63
	ds_write_b16_d16_hi v155, v82 offset:45184
	s_waitcnt lgkmcnt(15)
	v_lshlrev_b32_e32 v83, 16, v83
	v_fma_f32 v83, v231, v83, v17
	v_bfe_u32 v206, v83, 16, 1
	v_add3_u32 v83, v83, v206, s63
	ds_write_b16_d16_hi v155, v83 offset:45248
	s_waitcnt lgkmcnt(15)
	v_lshlrev_b32_e32 v84, 16, v84
	v_fma_f32 v84, v231, v84, v2
	v_bfe_u32 v206, v84, 16, 1
	v_add3_u32 v84, v84, v206, s63
	ds_write_b16_d16_hi v155, v84 offset:45376
	s_waitcnt lgkmcnt(15)
	v_lshlrev_b32_e32 v85, 16, v85
	v_fma_f32 v85, v231, v85, v18
	v_bfe_u32 v206, v85, 16, 1
	v_add3_u32 v85, v85, v206, s63
	ds_write_b16_d16_hi v155, v85 offset:45312
	s_waitcnt lgkmcnt(15)
	v_lshlrev_b32_e32 v86, 16, v86
	v_fma_f32 v86, v231, v86, v3
	v_bfe_u32 v206, v86, 16, 1
	v_add3_u32 v86, v86, v206, s63
	ds_write_b16_d16_hi v155, v86 offset:45504
	s_waitcnt lgkmcnt(15)
	v_lshlrev_b32_e32 v87, 16, v87
	v_fma_f32 v87, v231, v87, v19
	v_bfe_u32 v206, v87, 16, 1
	v_add3_u32 v87, v87, v206, s63
	ds_write_b16_d16_hi v155, v87 offset:45440
	s_waitcnt lgkmcnt(15)
	v_lshlrev_b32_e32 v88, 16, v88
	v_fma_f32 v88, v231, v88, v4
	v_bfe_u32 v206, v88, 16, 1
	v_add3_u32 v88, v88, v206, s63
	ds_write_b16_d16_hi v155, v88 offset:46080
	s_waitcnt lgkmcnt(15)
	v_lshlrev_b32_e32 v89, 16, v89
	v_fma_f32 v89, v231, v89, v20
	v_bfe_u32 v206, v89, 16, 1
	v_add3_u32 v89, v89, v206, s63
	ds_write_b16_d16_hi v155, v89 offset:46144
	s_waitcnt lgkmcnt(15)
	v_lshlrev_b32_e32 v90, 16, v90
	v_fma_f32 v90, v231, v90, v5
	v_bfe_u32 v206, v90, 16, 1
	v_add3_u32 v90, v90, v206, s63
	ds_write_b16_d16_hi v155, v90 offset:46208
	s_waitcnt lgkmcnt(15)
	v_lshlrev_b32_e32 v91, 16, v91
	v_fma_f32 v91, v231, v91, v21
	v_bfe_u32 v206, v91, 16, 1
	v_add3_u32 v91, v91, v206, s63
	ds_write_b16_d16_hi v155, v91 offset:46272
	s_waitcnt lgkmcnt(15)
	v_lshlrev_b32_e32 v92, 16, v92
	v_fma_f32 v92, v231, v92, v6
	v_bfe_u32 v206, v92, 16, 1
	v_add3_u32 v92, v92, v206, s63
	ds_write_b16_d16_hi v155, v92 offset:46400
	s_waitcnt lgkmcnt(15)
	v_lshlrev_b32_e32 v93, 16, v93
	v_fma_f32 v93, v231, v93, v22
	v_bfe_u32 v206, v93, 16, 1
	v_add3_u32 v93, v93, v206, s63
	ds_write_b16_d16_hi v155, v93 offset:46336
	s_waitcnt lgkmcnt(15)
	v_lshlrev_b32_e32 v94, 16, v94
	v_fma_f32 v94, v231, v94, v7
	v_bfe_u32 v206, v94, 16, 1
	v_add3_u32 v94, v94, v206, s63
	ds_write_b16_d16_hi v155, v94 offset:46528
	s_waitcnt lgkmcnt(15)
	v_lshlrev_b32_e32 v95, 16, v95
	v_fma_f32 v95, v231, v95, v23
	v_bfe_u32 v206, v95, 16, 1
	v_add3_u32 v95, v95, v206, s63
	ds_write_b16_d16_hi v155, v95 offset:46464
	ds_read_u16 v80, v155 offset:47104
	ds_read_u16 v81, v155 offset:47168
	ds_read_u16 v82, v155 offset:47232
	ds_read_u16 v83, v155 offset:47296
	ds_read_u16 v84, v155 offset:47424
	ds_read_u16 v85, v155 offset:47360
	ds_read_u16 v86, v155 offset:47552
	ds_read_u16 v87, v155 offset:47488
	ds_read_u16 v88, v155 offset:48128
	ds_read_u16 v89, v155 offset:48192
	ds_read_u16 v90, v155 offset:48256
	ds_read_u16 v91, v155 offset:48320
	ds_read_u16 v92, v155 offset:48448
	ds_read_u16 v93, v155 offset:48384
	ds_read_u16 v94, v155 offset:48576
	ds_read_u16 v95, v155 offset:48512
	s_waitcnt lgkmcnt(15)
	v_lshlrev_b32_e32 v80, 16, v80
	v_fma_f32 v80, v231, v80, v8
	v_bfe_u32 v206, v80, 16, 1
	v_add3_u32 v80, v80, v206, s63
	ds_write_b16_d16_hi v155, v80 offset:47104
	s_waitcnt lgkmcnt(15)
	v_lshlrev_b32_e32 v81, 16, v81
	v_fma_f32 v81, v231, v81, v24
	v_bfe_u32 v206, v81, 16, 1
	v_add3_u32 v81, v81, v206, s63
	ds_write_b16_d16_hi v155, v81 offset:47168
	s_waitcnt lgkmcnt(15)
	v_lshlrev_b32_e32 v82, 16, v82
	v_fma_f32 v82, v231, v82, v9
	v_bfe_u32 v206, v82, 16, 1
	v_add3_u32 v82, v82, v206, s63
	ds_write_b16_d16_hi v155, v82 offset:47232
	s_waitcnt lgkmcnt(15)
	v_lshlrev_b32_e32 v83, 16, v83
	v_fma_f32 v83, v231, v83, v25
	v_bfe_u32 v206, v83, 16, 1
	v_add3_u32 v83, v83, v206, s63
	ds_write_b16_d16_hi v155, v83 offset:47296
	s_waitcnt lgkmcnt(15)
	v_lshlrev_b32_e32 v84, 16, v84
	v_fma_f32 v84, v231, v84, v10
	v_bfe_u32 v206, v84, 16, 1
	v_add3_u32 v84, v84, v206, s63
	ds_write_b16_d16_hi v155, v84 offset:47424
	s_waitcnt lgkmcnt(15)
	v_lshlrev_b32_e32 v85, 16, v85
	v_fma_f32 v85, v231, v85, v26
	v_bfe_u32 v206, v85, 16, 1
	v_add3_u32 v85, v85, v206, s63
	ds_write_b16_d16_hi v155, v85 offset:47360
	s_waitcnt lgkmcnt(15)
	v_lshlrev_b32_e32 v86, 16, v86
	v_fma_f32 v86, v231, v86, v11
	v_bfe_u32 v206, v86, 16, 1
	v_add3_u32 v86, v86, v206, s63
	ds_write_b16_d16_hi v155, v86 offset:47552
	s_waitcnt lgkmcnt(15)
	v_lshlrev_b32_e32 v87, 16, v87
	v_fma_f32 v87, v231, v87, v27
	v_bfe_u32 v206, v87, 16, 1
	v_add3_u32 v87, v87, v206, s63
	ds_write_b16_d16_hi v155, v87 offset:47488
	s_waitcnt lgkmcnt(15)
	v_lshlrev_b32_e32 v88, 16, v88
	v_fma_f32 v88, v231, v88, v12
	v_bfe_u32 v206, v88, 16, 1
	v_add3_u32 v88, v88, v206, s63
	ds_write_b16_d16_hi v155, v88 offset:48128
	s_waitcnt lgkmcnt(15)
	v_lshlrev_b32_e32 v89, 16, v89
	v_fma_f32 v89, v231, v89, v28
	v_bfe_u32 v206, v89, 16, 1
	v_add3_u32 v89, v89, v206, s63
	ds_write_b16_d16_hi v155, v89 offset:48192
	s_waitcnt lgkmcnt(15)
	v_lshlrev_b32_e32 v90, 16, v90
	v_fma_f32 v90, v231, v90, v13
	v_bfe_u32 v206, v90, 16, 1
	v_add3_u32 v90, v90, v206, s63
	ds_write_b16_d16_hi v155, v90 offset:48256
	s_waitcnt lgkmcnt(15)
	v_lshlrev_b32_e32 v91, 16, v91
	v_fma_f32 v91, v231, v91, v29
	v_bfe_u32 v206, v91, 16, 1
	v_add3_u32 v91, v91, v206, s63
	ds_write_b16_d16_hi v155, v91 offset:48320
	s_waitcnt lgkmcnt(15)
	v_lshlrev_b32_e32 v92, 16, v92
	v_fma_f32 v92, v231, v92, v14
	v_bfe_u32 v206, v92, 16, 1
	v_add3_u32 v92, v92, v206, s63
	ds_write_b16_d16_hi v155, v92 offset:48448
	s_waitcnt lgkmcnt(15)
	v_lshlrev_b32_e32 v93, 16, v93
	v_fma_f32 v93, v231, v93, v30
	v_bfe_u32 v206, v93, 16, 1
	v_add3_u32 v93, v93, v206, s63
	ds_write_b16_d16_hi v155, v93 offset:48384
	s_waitcnt lgkmcnt(15)
	v_lshlrev_b32_e32 v94, 16, v94
	v_fma_f32 v94, v231, v94, v15
	v_bfe_u32 v206, v94, 16, 1
	v_add3_u32 v94, v94, v206, s63
	ds_write_b16_d16_hi v155, v94 offset:48576
	s_waitcnt lgkmcnt(15)
	v_lshlrev_b32_e32 v95, 16, v95
	v_fma_f32 v95, v231, v95, v31
	v_bfe_u32 v206, v95, 16, 1
	v_add3_u32 v95, v95, v206, s63
	ds_write_b16_d16_hi v155, v95 offset:48512
	v_mov_b64_e32 v[0:1], s[10:11]
	v_mad_u64_u32 v[0:1], s[12:13], v201, s62, v[0:1]
	v_lshl_add_u64 v[60:61], s[94:95], 1, v[0:1]
	v_add_co_u32_e32 v0, vcc, s82, v60
	s_mov_b64 s[12:13], 0x1000
	s_nop 0
	v_addc_co_u32_e32 v1, vcc, 0, v61, vcc
	v_lshl_add_u64 v[4:5], v[60:61], 0, s[12:13]
	s_waitcnt vmcnt(0)
	v_mov_b64_e32 v[52:53], v[210:211]
	v_mov_b64_e32 v[54:55], v[212:213]
	v_mov_b64_e32 v[24:25], v[214:215]
	v_mov_b64_e32 v[26:27], v[216:217]
	v_mov_b64_e32 v[40:41], v[218:219]
	v_mov_b64_e32 v[42:43], v[220:221]
	v_mov_b64_e32 v[48:49], v[226:227]
	v_mov_b64_e32 v[50:51], v[228:229]
	v_mov_b64_e32 v[0:1], v[232:233]
	v_mov_b64_e32 v[2:3], v[234:235]
	v_mov_b64_e32 v[8:9], v[236:237]
	v_mov_b64_e32 v[10:11], v[238:239]
	v_mov_b64_e32 v[16:17], v[240:241]
	v_mov_b64_e32 v[18:19], v[242:243]
	v_mov_b64_e32 v[28:29], v[244:245]
	v_mov_b64_e32 v[30:31], v[246:247]
	ds_read_b128 v[64:67], v197 offset:40960
	ds_read_b128 v[56:59], v197 offset:40976
	ds_read_b128 v[44:47], v197 offset:40992
	ds_read_b128 v[36:39], v197 offset:41008
	ds_read_b128 v[32:35], v198 offset:40960
	ds_read_b128 v[20:23], v198 offset:40976
	ds_read_b128 v[12:15], v198 offset:40992
	ds_read_b128 v[4:7], v198 offset:41008
	s_waitcnt lgkmcnt(7)
	v_lshlrev_b32_e32 v62, 16, v64
	v_and_b32_e32 v63, 0xffff0000, v64
	v_lshlrev_b32_e32 v64, 16, v65
	v_and_b32_e32 v65, 0xffff0000, v65
	s_waitcnt vmcnt(7)
	v_lshlrev_b32_e32 v68, 16, v52
	v_and_b32_e32 v69, 0xffff0000, v52
	v_mul_f32_e32 v52, 0xbfb8aa3b, v68
	v_lshlrev_b32_e32 v72, 16, v54
	v_exp_f32_e32 v52, v52
	v_and_b32_e32 v73, 0xffff0000, v54
	v_mul_f32_e32 v54, 0xbfb8aa3b, v72
	v_exp_f32_e32 v54, v54
	v_add_f32_e32 v52, 1.0, v52
	v_rcp_f32_e32 v70, v52
	v_mul_f32_e32 v52, 0xbfb8aa3b, v69
	v_add_f32_e32 v54, 1.0, v54
	v_exp_f32_e32 v52, v52
	v_rcp_f32_e32 v74, v54
	v_mul_f32_e32 v54, 0xbfb8aa3b, v73
	v_exp_f32_e32 v54, v54
	v_add_f32_e32 v52, 1.0, v52
	v_rcp_f32_e32 v71, v52
	v_lshlrev_b32_e32 v52, 16, v53
	v_add_f32_e32 v54, 1.0, v54
	v_rcp_f32_e32 v75, v54
	v_and_b32_e32 v53, 0xffff0000, v53
	v_pk_mul_f32 v[68:69], v[70:71], v[68:69]
	v_mul_f32_e32 v70, 0xbfb8aa3b, v52
	v_mul_f32_e32 v71, 0xbfb8aa3b, v53
	v_lshlrev_b32_e32 v54, 16, v55
	v_and_b32_e32 v55, 0xffff0000, v55
	v_exp_f32_e32 v70, v70
	v_exp_f32_e32 v71, v71
	v_pk_mul_f32 v[72:73], v[74:75], v[72:73]
	v_mul_f32_e32 v74, 0xbfb8aa3b, v54
	v_mul_f32_e32 v75, 0xbfb8aa3b, v55
	v_exp_f32_e32 v74, v74
	v_exp_f32_e32 v75, v75
	v_add_f32_e32 v70, 1.0, v70
	v_add_f32_e32 v71, 1.0, v71
	v_rcp_f32_e32 v70, v70
	v_rcp_f32_e32 v71, v71
	v_add_f32_e32 v74, 1.0, v74
	v_add_f32_e32 v75, 1.0, v75
	v_rcp_f32_e32 v74, v74
	v_rcp_f32_e32 v75, v75
	v_pk_mul_f32 v[52:53], v[70:71], v[52:53]
	v_pk_mul_f32 v[68:69], v[68:69], v[62:63]
	v_pk_mul_f32 v[70:71], v[52:53], v[64:65]
	v_lshlrev_b32_e32 v64, 16, v66
	v_and_b32_e32 v65, 0xffff0000, v66
	v_lshlrev_b32_e32 v66, 16, v67
	v_and_b32_e32 v67, 0xffff0000, v67
	v_pk_mul_f32 v[54:55], v[74:75], v[54:55]
	v_pk_mul_f32 v[72:73], v[72:73], v[64:65]
	v_pk_mul_f32 v[74:75], v[54:55], v[66:67]
	v_pk_mul_f32 v[62:63], v[68:69], v[68:69]
	v_cvt_pk_bf16_f32 v66, v68, v69
	v_cvt_pk_bf16_f32 v67, v70, v71
	v_cvt_pk_bf16_f32 v68, v72, v73
	v_cvt_pk_bf16_f32 v69, v74, v75
	global_store_dwordx4 v[60:61], v[66:69], off offset:2048
	v_pk_mul_f32 v[64:65], v[72:73], v[72:73]
	s_waitcnt vmcnt(5)
	v_lshlrev_b32_e32 v72, 16, v50
	v_lshlrev_b32_e32 v68, 16, v48
	v_and_b32_e32 v69, 0xffff0000, v48
	v_mul_f32_e32 v48, 0xbfb8aa3b, v68
	v_exp_f32_e32 v48, v48
	v_and_b32_e32 v73, 0xffff0000, v50
	v_mul_f32_e32 v50, 0xbfb8aa3b, v72
	v_exp_f32_e32 v50, v50
	v_add_f32_e32 v48, 1.0, v48
	v_pk_mul_f32 v[52:53], v[70:71], v[70:71]
	v_rcp_f32_e32 v70, v48
	v_mul_f32_e32 v48, 0xbfb8aa3b, v69
	v_add_f32_e32 v50, 1.0, v50
	v_pk_mul_f32 v[54:55], v[74:75], v[74:75]
	v_exp_f32_e32 v48, v48
	v_rcp_f32_e32 v74, v50
	v_mul_f32_e32 v50, 0xbfb8aa3b, v73
	v_exp_f32_e32 v50, v50
	v_add_f32_e32 v48, 1.0, v48
	v_rcp_f32_e32 v71, v48
	v_lshlrev_b32_e32 v48, 16, v49
	v_add_f32_e32 v50, 1.0, v50
	v_rcp_f32_e32 v75, v50
	v_and_b32_e32 v49, 0xffff0000, v49
	v_pk_mul_f32 v[68:69], v[70:71], v[68:69]
	v_mul_f32_e32 v70, 0xbfb8aa3b, v48
	v_mul_f32_e32 v71, 0xbfb8aa3b, v49
	v_lshlrev_b32_e32 v50, 16, v51
	v_and_b32_e32 v51, 0xffff0000, v51
	v_exp_f32_e32 v70, v70
	v_exp_f32_e32 v71, v71
	v_pk_mul_f32 v[72:73], v[74:75], v[72:73]
	v_mul_f32_e32 v74, 0xbfb8aa3b, v50
	v_mul_f32_e32 v75, 0xbfb8aa3b, v51
	v_exp_f32_e32 v74, v74
	v_exp_f32_e32 v75, v75
	v_add_f32_e32 v70, 1.0, v70
	v_add_f32_e32 v71, 1.0, v71
	v_rcp_f32_e32 v70, v70
	v_rcp_f32_e32 v71, v71
	v_add_f32_e32 v74, 1.0, v74
	v_add_f32_e32 v75, 1.0, v75
	v_rcp_f32_e32 v74, v74
	v_rcp_f32_e32 v75, v75
	s_waitcnt lgkmcnt(6)
	v_lshlrev_b32_e32 v66, 16, v56
	v_and_b32_e32 v67, 0xffff0000, v56
	v_lshlrev_b32_e32 v56, 16, v57
	v_and_b32_e32 v57, 0xffff0000, v57
	v_pk_mul_f32 v[48:49], v[70:71], v[48:49]
	v_pk_mul_f32 v[50:51], v[74:75], v[50:51]
	v_pk_mul_f32 v[70:71], v[48:49], v[56:57]
	v_lshlrev_b32_e32 v56, 16, v58
	v_and_b32_e32 v57, 0xffff0000, v58
	v_lshlrev_b32_e32 v58, 16, v59
	v_and_b32_e32 v59, 0xffff0000, v59
	v_pk_mul_f32 v[68:69], v[68:69], v[66:67]
	v_pk_mul_f32 v[72:73], v[72:73], v[56:57]
	v_pk_mul_f32 v[58:59], v[50:51], v[58:59]
	v_pk_mul_f32 v[66:67], v[68:69], v[68:69]
	v_pk_mul_f32 v[48:49], v[70:71], v[70:71]
	v_cvt_pk_bf16_f32 v68, v68, v69
	v_cvt_pk_bf16_f32 v69, v70, v71
	v_cvt_pk_bf16_f32 v70, v72, v73
	v_cvt_pk_bf16_f32 v71, v58, v59
	global_store_dwordx4 v[60:61], v[68:71], off offset:2064
	v_pk_mul_f32 v[56:57], v[72:73], v[72:73]
	v_lshlrev_b32_e32 v72, 16, v42
	v_lshlrev_b32_e32 v68, 16, v40
	v_and_b32_e32 v69, 0xffff0000, v40
	v_mul_f32_e32 v40, 0xbfb8aa3b, v68
	v_exp_f32_e32 v40, v40
	v_and_b32_e32 v73, 0xffff0000, v42
	v_mul_f32_e32 v42, 0xbfb8aa3b, v72
	v_exp_f32_e32 v42, v42
	v_add_f32_e32 v40, 1.0, v40
	v_rcp_f32_e32 v70, v40
	v_mul_f32_e32 v40, 0xbfb8aa3b, v69
	v_add_f32_e32 v42, 1.0, v42
	v_exp_f32_e32 v40, v40
	v_rcp_f32_e32 v74, v42
	v_mul_f32_e32 v42, 0xbfb8aa3b, v73
	v_exp_f32_e32 v42, v42
	v_add_f32_e32 v40, 1.0, v40
	v_rcp_f32_e32 v71, v40
	v_lshlrev_b32_e32 v40, 16, v41
	v_add_f32_e32 v42, 1.0, v42
	v_rcp_f32_e32 v75, v42
	v_and_b32_e32 v41, 0xffff0000, v41
	v_pk_mul_f32 v[68:69], v[70:71], v[68:69]
	v_mul_f32_e32 v70, 0xbfb8aa3b, v40
	v_mul_f32_e32 v71, 0xbfb8aa3b, v41
	v_lshlrev_b32_e32 v42, 16, v43
	v_and_b32_e32 v43, 0xffff0000, v43
	v_exp_f32_e32 v70, v70
	v_exp_f32_e32 v71, v71
	v_pk_mul_f32 v[72:73], v[74:75], v[72:73]
	v_mul_f32_e32 v74, 0xbfb8aa3b, v42
	v_mul_f32_e32 v75, 0xbfb8aa3b, v43
	v_exp_f32_e32 v74, v74
	v_exp_f32_e32 v75, v75
	v_add_f32_e32 v70, 1.0, v70
	v_add_f32_e32 v71, 1.0, v71
	v_rcp_f32_e32 v70, v70
	v_rcp_f32_e32 v71, v71
	v_add_f32_e32 v74, 1.0, v74
	v_add_f32_e32 v75, 1.0, v75
	v_rcp_f32_e32 v74, v74
	v_rcp_f32_e32 v75, v75
	v_pk_mul_f32 v[50:51], v[58:59], v[58:59]
	s_waitcnt lgkmcnt(5)
	v_lshlrev_b32_e32 v58, 16, v44
	v_and_b32_e32 v59, 0xffff0000, v44
	v_lshlrev_b32_e32 v44, 16, v45
	v_and_b32_e32 v45, 0xffff0000, v45
	v_pk_mul_f32 v[40:41], v[70:71], v[40:41]
	v_pk_mul_f32 v[42:43], v[74:75], v[42:43]
	v_pk_mul_f32 v[70:71], v[40:41], v[44:45]
	v_lshlrev_b32_e32 v44, 16, v46
	v_and_b32_e32 v45, 0xffff0000, v46
	v_lshlrev_b32_e32 v46, 16, v47
	v_and_b32_e32 v47, 0xffff0000, v47
	v_pk_mul_f32 v[68:69], v[68:69], v[58:59]
	v_pk_mul_f32 v[72:73], v[72:73], v[44:45]
	v_pk_mul_f32 v[46:47], v[42:43], v[46:47]
	v_pk_mul_f32 v[58:59], v[68:69], v[68:69]
	v_pk_mul_f32 v[40:41], v[70:71], v[70:71]
	v_cvt_pk_bf16_f32 v68, v68, v69
	v_cvt_pk_bf16_f32 v69, v70, v71
	v_cvt_pk_bf16_f32 v70, v72, v73
	v_cvt_pk_bf16_f32 v71, v46, v47
	global_store_dwordx4 v[60:61], v[68:71], off offset:2080
	v_pk_mul_f32 v[44:45], v[72:73], v[72:73]
	v_lshlrev_b32_e32 v72, 16, v26
	v_lshlrev_b32_e32 v68, 16, v24
	v_and_b32_e32 v69, 0xffff0000, v24
	v_mul_f32_e32 v24, 0xbfb8aa3b, v68
	v_exp_f32_e32 v24, v24
	v_and_b32_e32 v73, 0xffff0000, v26
	v_mul_f32_e32 v26, 0xbfb8aa3b, v72
	v_exp_f32_e32 v26, v26
	v_add_f32_e32 v24, 1.0, v24
	v_rcp_f32_e32 v70, v24
	v_mul_f32_e32 v24, 0xbfb8aa3b, v69
	v_add_f32_e32 v26, 1.0, v26
	v_exp_f32_e32 v24, v24
	v_rcp_f32_e32 v74, v26
	v_mul_f32_e32 v26, 0xbfb8aa3b, v73
	v_exp_f32_e32 v26, v26
	v_add_f32_e32 v24, 1.0, v24
	v_rcp_f32_e32 v71, v24
	v_lshlrev_b32_e32 v24, 16, v25
	v_add_f32_e32 v26, 1.0, v26
	v_rcp_f32_e32 v75, v26
	v_and_b32_e32 v25, 0xffff0000, v25
	v_pk_mul_f32 v[68:69], v[70:71], v[68:69]
	v_mul_f32_e32 v70, 0xbfb8aa3b, v24
	v_mul_f32_e32 v71, 0xbfb8aa3b, v25
	v_lshlrev_b32_e32 v26, 16, v27
	v_and_b32_e32 v27, 0xffff0000, v27
	v_exp_f32_e32 v70, v70
	v_exp_f32_e32 v71, v71
	v_pk_mul_f32 v[72:73], v[74:75], v[72:73]
	v_mul_f32_e32 v74, 0xbfb8aa3b, v26
	v_mul_f32_e32 v75, 0xbfb8aa3b, v27
	v_exp_f32_e32 v74, v74
	v_exp_f32_e32 v75, v75
	v_add_f32_e32 v70, 1.0, v70
	v_add_f32_e32 v71, 1.0, v71
	v_rcp_f32_e32 v70, v70
	v_rcp_f32_e32 v71, v71
	v_add_f32_e32 v74, 1.0, v74
	v_add_f32_e32 v75, 1.0, v75
	v_rcp_f32_e32 v74, v74
	v_rcp_f32_e32 v75, v75
	v_pk_mul_f32 v[42:43], v[46:47], v[46:47]
	s_waitcnt lgkmcnt(4)
	v_lshlrev_b32_e32 v46, 16, v36
	v_and_b32_e32 v47, 0xffff0000, v36
	v_lshlrev_b32_e32 v36, 16, v37
	v_and_b32_e32 v37, 0xffff0000, v37
	v_pk_mul_f32 v[24:25], v[70:71], v[24:25]
	v_pk_mul_f32 v[26:27], v[74:75], v[26:27]
	v_pk_mul_f32 v[70:71], v[24:25], v[36:37]
	v_lshlrev_b32_e32 v36, 16, v38
	v_and_b32_e32 v37, 0xffff0000, v38
	v_lshlrev_b32_e32 v38, 16, v39
	v_and_b32_e32 v39, 0xffff0000, v39
	v_pk_mul_f32 v[68:69], v[68:69], v[46:47]
	v_pk_mul_f32 v[72:73], v[72:73], v[36:37]
	v_pk_mul_f32 v[38:39], v[26:27], v[38:39]
	v_pk_mul_f32 v[46:47], v[68:69], v[68:69]
	v_pk_mul_f32 v[24:25], v[70:71], v[70:71]
	v_cvt_pk_bf16_f32 v68, v68, v69
	v_cvt_pk_bf16_f32 v69, v70, v71
	v_cvt_pk_bf16_f32 v70, v72, v73
	v_cvt_pk_bf16_f32 v71, v38, v39
	global_store_dwordx4 v[60:61], v[68:71], off offset:2096
	v_pk_mul_f32 v[36:37], v[72:73], v[72:73]
	s_waitcnt vmcnt(4)
	v_lshlrev_b32_e32 v72, 16, v30
	v_lshlrev_b32_e32 v68, 16, v28
	v_and_b32_e32 v69, 0xffff0000, v28
	v_mul_f32_e32 v28, 0xbfb8aa3b, v68
	v_exp_f32_e32 v28, v28
	v_and_b32_e32 v73, 0xffff0000, v30
	v_mul_f32_e32 v30, 0xbfb8aa3b, v72
	v_exp_f32_e32 v30, v30
	v_add_f32_e32 v28, 1.0, v28
	v_rcp_f32_e32 v70, v28
	v_mul_f32_e32 v28, 0xbfb8aa3b, v69
	v_add_f32_e32 v30, 1.0, v30
	v_exp_f32_e32 v28, v28
	v_rcp_f32_e32 v74, v30
	v_mul_f32_e32 v30, 0xbfb8aa3b, v73
	v_exp_f32_e32 v30, v30
	v_add_f32_e32 v28, 1.0, v28
	v_rcp_f32_e32 v71, v28
	v_lshlrev_b32_e32 v28, 16, v29
	v_add_f32_e32 v30, 1.0, v30
	v_rcp_f32_e32 v75, v30
	v_and_b32_e32 v29, 0xffff0000, v29
	v_pk_mul_f32 v[68:69], v[70:71], v[68:69]
	v_mul_f32_e32 v70, 0xbfb8aa3b, v28
	v_mul_f32_e32 v71, 0xbfb8aa3b, v29
	v_lshlrev_b32_e32 v30, 16, v31
	v_and_b32_e32 v31, 0xffff0000, v31
	v_exp_f32_e32 v70, v70
	v_exp_f32_e32 v71, v71
	v_pk_mul_f32 v[72:73], v[74:75], v[72:73]
	v_mul_f32_e32 v74, 0xbfb8aa3b, v30
	v_mul_f32_e32 v75, 0xbfb8aa3b, v31
	v_exp_f32_e32 v74, v74
	v_exp_f32_e32 v75, v75
	v_add_f32_e32 v70, 1.0, v70
	v_add_f32_e32 v71, 1.0, v71
	v_rcp_f32_e32 v70, v70
	v_rcp_f32_e32 v71, v71
	v_add_f32_e32 v74, 1.0, v74
	v_add_f32_e32 v75, 1.0, v75
	v_rcp_f32_e32 v74, v74
	v_rcp_f32_e32 v75, v75
	v_pk_mul_f32 v[26:27], v[38:39], v[38:39]
	s_waitcnt lgkmcnt(3)
	v_lshlrev_b32_e32 v38, 16, v32
	v_and_b32_e32 v39, 0xffff0000, v32
	v_lshlrev_b32_e32 v32, 16, v33
	v_and_b32_e32 v33, 0xffff0000, v33
	v_pk_mul_f32 v[28:29], v[70:71], v[28:29]
	v_pk_mul_f32 v[30:31], v[74:75], v[30:31]
	v_pk_mul_f32 v[70:71], v[28:29], v[32:33]
	v_lshlrev_b32_e32 v32, 16, v34
	v_and_b32_e32 v33, 0xffff0000, v34
	v_lshlrev_b32_e32 v34, 16, v35
	v_and_b32_e32 v35, 0xffff0000, v35
	v_pk_mul_f32 v[68:69], v[68:69], v[38:39]
	v_pk_mul_f32 v[72:73], v[72:73], v[32:33]
	v_pk_mul_f32 v[34:35], v[30:31], v[34:35]
	v_pk_mul_f32 v[38:39], v[68:69], v[68:69]
	v_pk_mul_f32 v[28:29], v[70:71], v[70:71]
	v_cvt_pk_bf16_f32 v68, v68, v69
	v_cvt_pk_bf16_f32 v69, v70, v71
	v_cvt_pk_bf16_f32 v70, v72, v73
	v_cvt_pk_bf16_f32 v71, v34, v35
	global_store_dwordx4 v[60:61], v[68:71], off offset:2112
	v_pk_mul_f32 v[32:33], v[72:73], v[72:73]
	v_lshlrev_b32_e32 v72, 16, v18
	v_lshlrev_b32_e32 v68, 16, v16
	v_and_b32_e32 v69, 0xffff0000, v16
	v_mul_f32_e32 v16, 0xbfb8aa3b, v68
	v_exp_f32_e32 v16, v16
	v_and_b32_e32 v73, 0xffff0000, v18
	v_mul_f32_e32 v18, 0xbfb8aa3b, v72
	v_exp_f32_e32 v18, v18
	v_add_f32_e32 v16, 1.0, v16
	v_rcp_f32_e32 v70, v16
	v_mul_f32_e32 v16, 0xbfb8aa3b, v69
	v_add_f32_e32 v18, 1.0, v18
	v_exp_f32_e32 v16, v16
	v_rcp_f32_e32 v74, v18
	v_mul_f32_e32 v18, 0xbfb8aa3b, v73
	v_exp_f32_e32 v18, v18
	v_add_f32_e32 v16, 1.0, v16
	v_rcp_f32_e32 v71, v16
	v_lshlrev_b32_e32 v16, 16, v17
	v_add_f32_e32 v18, 1.0, v18
	v_rcp_f32_e32 v75, v18
	v_and_b32_e32 v17, 0xffff0000, v17
	v_pk_mul_f32 v[68:69], v[70:71], v[68:69]
	v_mul_f32_e32 v70, 0xbfb8aa3b, v16
	v_mul_f32_e32 v71, 0xbfb8aa3b, v17
	v_lshlrev_b32_e32 v18, 16, v19
	v_and_b32_e32 v19, 0xffff0000, v19
	v_exp_f32_e32 v70, v70
	v_exp_f32_e32 v71, v71
	v_pk_mul_f32 v[72:73], v[74:75], v[72:73]
	v_mul_f32_e32 v74, 0xbfb8aa3b, v18
	v_mul_f32_e32 v75, 0xbfb8aa3b, v19
	v_exp_f32_e32 v74, v74
	v_exp_f32_e32 v75, v75
	v_add_f32_e32 v70, 1.0, v70
	v_add_f32_e32 v71, 1.0, v71
	v_rcp_f32_e32 v70, v70
	v_rcp_f32_e32 v71, v71
	v_add_f32_e32 v74, 1.0, v74
	v_add_f32_e32 v75, 1.0, v75
	v_rcp_f32_e32 v74, v74
	v_rcp_f32_e32 v75, v75
	v_pk_mul_f32 v[30:31], v[34:35], v[34:35]
	s_waitcnt lgkmcnt(2)
	v_lshlrev_b32_e32 v34, 16, v20
	v_and_b32_e32 v35, 0xffff0000, v20
	v_lshlrev_b32_e32 v20, 16, v21
	v_and_b32_e32 v21, 0xffff0000, v21
	v_pk_mul_f32 v[16:17], v[70:71], v[16:17]
	v_pk_mul_f32 v[18:19], v[74:75], v[18:19]
	v_pk_mul_f32 v[70:71], v[16:17], v[20:21]
	v_lshlrev_b32_e32 v20, 16, v22
	v_and_b32_e32 v21, 0xffff0000, v22
	v_lshlrev_b32_e32 v22, 16, v23
	v_and_b32_e32 v23, 0xffff0000, v23
	v_pk_mul_f32 v[68:69], v[68:69], v[34:35]
	v_pk_mul_f32 v[72:73], v[72:73], v[20:21]
	v_pk_mul_f32 v[22:23], v[18:19], v[22:23]
	v_pk_mul_f32 v[34:35], v[68:69], v[68:69]
	v_pk_mul_f32 v[16:17], v[70:71], v[70:71]
	v_cvt_pk_bf16_f32 v68, v68, v69
	v_cvt_pk_bf16_f32 v69, v70, v71
	v_cvt_pk_bf16_f32 v70, v72, v73
	v_cvt_pk_bf16_f32 v71, v22, v23
	global_store_dwordx4 v[60:61], v[68:71], off offset:2128
	v_pk_mul_f32 v[20:21], v[72:73], v[72:73]
	v_lshlrev_b32_e32 v72, 16, v10
	v_lshlrev_b32_e32 v68, 16, v8
	v_and_b32_e32 v69, 0xffff0000, v8
	v_mul_f32_e32 v8, 0xbfb8aa3b, v68
	v_exp_f32_e32 v8, v8
	v_and_b32_e32 v73, 0xffff0000, v10
	v_mul_f32_e32 v10, 0xbfb8aa3b, v72
	v_exp_f32_e32 v10, v10
	v_add_f32_e32 v62, v62, v63
	v_add_f32_e32 v52, v52, v62
	v_add_f32_e32 v8, 1.0, v8
	v_add_f32_e32 v52, v53, v52
	v_rcp_f32_e32 v70, v8
	v_mul_f32_e32 v8, 0xbfb8aa3b, v69
	v_add_f32_e32 v10, 1.0, v10
	v_add_f32_e32 v52, v64, v52
	v_exp_f32_e32 v8, v8
	v_rcp_f32_e32 v74, v10
	v_mul_f32_e32 v10, 0xbfb8aa3b, v73
	v_add_f32_e32 v52, v65, v52
	v_exp_f32_e32 v10, v10
	v_add_f32_e32 v52, v54, v52
	v_add_f32_e32 v52, v55, v52
	v_add_f32_e32 v52, v66, v52
	v_add_f32_e32 v8, 1.0, v8
	v_add_f32_e32 v52, v67, v52
	v_rcp_f32_e32 v71, v8
	v_add_f32_e32 v10, 1.0, v10
	v_add_f32_e32 v48, v48, v52
	v_rcp_f32_e32 v75, v10
	v_add_f32_e32 v48, v49, v48
	v_add_f32_e32 v48, v56, v48
	v_lshlrev_b32_e32 v8, 16, v9
	v_and_b32_e32 v9, 0xffff0000, v9
	v_add_f32_e32 v48, v57, v48
	v_pk_mul_f32 v[68:69], v[70:71], v[68:69]
	v_mul_f32_e32 v70, 0xbfb8aa3b, v8
	v_mul_f32_e32 v71, 0xbfb8aa3b, v9
	v_lshlrev_b32_e32 v10, 16, v11
	v_and_b32_e32 v11, 0xffff0000, v11
	v_add_f32_e32 v48, v50, v48
	v_exp_f32_e32 v70, v70
	v_exp_f32_e32 v71, v71
	v_pk_mul_f32 v[72:73], v[74:75], v[72:73]
	v_mul_f32_e32 v74, 0xbfb8aa3b, v10
	v_mul_f32_e32 v75, 0xbfb8aa3b, v11
	v_add_f32_e32 v48, v51, v48
	v_exp_f32_e32 v74, v74
	v_exp_f32_e32 v75, v75
	v_add_f32_e32 v48, v58, v48
	v_add_f32_e32 v48, v59, v48
	v_add_f32_e32 v40, v40, v48
	v_add_f32_e32 v70, 1.0, v70
	v_add_f32_e32 v71, 1.0, v71
	v_add_f32_e32 v40, v41, v40
	v_rcp_f32_e32 v70, v70
	v_rcp_f32_e32 v71, v71
	v_add_f32_e32 v74, 1.0, v74
	v_add_f32_e32 v75, 1.0, v75
	v_add_f32_e32 v40, v44, v40
	v_rcp_f32_e32 v74, v74
	v_rcp_f32_e32 v75, v75
	v_add_f32_e32 v40, v45, v40
	v_add_f32_e32 v40, v42, v40
	v_add_f32_e32 v40, v43, v40
	v_pk_mul_f32 v[18:19], v[22:23], v[22:23]
	s_waitcnt lgkmcnt(1)
	v_lshlrev_b32_e32 v22, 16, v12
	v_and_b32_e32 v23, 0xffff0000, v12
	v_lshlrev_b32_e32 v12, 16, v13
	v_and_b32_e32 v13, 0xffff0000, v13
	v_pk_mul_f32 v[8:9], v[70:71], v[8:9]
	v_add_f32_e32 v40, v46, v40
	v_pk_mul_f32 v[70:71], v[8:9], v[12:13]
	v_lshlrev_b32_e32 v12, 16, v14
	v_and_b32_e32 v13, 0xffff0000, v14
	v_lshlrev_b32_e32 v14, 16, v15
	v_and_b32_e32 v15, 0xffff0000, v15
	v_pk_mul_f32 v[10:11], v[74:75], v[10:11]
	v_add_f32_e32 v40, v47, v40
	v_pk_mul_f32 v[68:69], v[68:69], v[22:23]
	v_pk_mul_f32 v[72:73], v[72:73], v[12:13]
	v_pk_mul_f32 v[14:15], v[10:11], v[14:15]
	v_add_f32_e32 v24, v24, v40
	v_pk_mul_f32 v[22:23], v[68:69], v[68:69]
	v_pk_mul_f32 v[8:9], v[70:71], v[70:71]
	v_cvt_pk_bf16_f32 v68, v68, v69
	v_cvt_pk_bf16_f32 v69, v70, v71
	v_cvt_pk_bf16_f32 v70, v72, v73
	v_cvt_pk_bf16_f32 v71, v14, v15
	v_add_f32_e32 v24, v25, v24
	global_store_dwordx4 v[60:61], v[68:71], off offset:2144
	v_add_f32_e32 v24, v36, v24
	v_add_f32_e32 v24, v37, v24
	v_lshlrev_b32_e32 v68, 16, v0
	v_and_b32_e32 v69, 0xffff0000, v0
	v_mul_f32_e32 v0, 0xbfb8aa3b, v68
	v_exp_f32_e32 v0, v0
	v_add_f32_e32 v24, v26, v24
	v_add_f32_e32 v24, v27, v24
	v_pk_mul_f32 v[12:13], v[72:73], v[72:73]
	v_lshlrev_b32_e32 v72, 16, v2
	v_add_f32_e32 v24, v38, v24
	v_and_b32_e32 v73, 0xffff0000, v2
	v_mul_f32_e32 v2, 0xbfb8aa3b, v72
	v_add_f32_e32 v24, v39, v24
	v_add_f32_e32 v0, 1.0, v0
	v_exp_f32_e32 v2, v2
	v_add_f32_e32 v24, v28, v24
	v_rcp_f32_e32 v70, v0
	v_mul_f32_e32 v0, 0xbfb8aa3b, v69
	v_add_f32_e32 v24, v29, v24
	v_exp_f32_e32 v0, v0
	v_add_f32_e32 v24, v32, v24
	v_add_f32_e32 v24, v33, v24
	v_add_f32_e32 v2, 1.0, v2
	v_add_f32_e32 v24, v30, v24
	v_rcp_f32_e32 v74, v2
	v_mul_f32_e32 v2, 0xbfb8aa3b, v73
	v_add_f32_e32 v24, v31, v24
	v_add_f32_e32 v0, 1.0, v0
	v_exp_f32_e32 v2, v2
	v_add_f32_e32 v24, v34, v24
	v_rcp_f32_e32 v71, v0
	v_add_f32_e32 v24, v35, v24
	v_add_f32_e32 v16, v16, v24
	v_add_f32_e32 v16, v17, v16
	v_lshlrev_b32_e32 v0, 16, v1
	v_and_b32_e32 v1, 0xffff0000, v1
	v_add_f32_e32 v2, 1.0, v2
	v_add_f32_e32 v16, v20, v16
	v_pk_mul_f32 v[68:69], v[70:71], v[68:69]
	v_mul_f32_e32 v70, 0xbfb8aa3b, v0
	v_mul_f32_e32 v71, 0xbfb8aa3b, v1
	v_rcp_f32_e32 v75, v2
	v_add_f32_e32 v16, v21, v16
	v_exp_f32_e32 v70, v70
	v_exp_f32_e32 v71, v71
	v_add_f32_e32 v16, v18, v16
	v_add_f32_e32 v16, v19, v16
	v_lshlrev_b32_e32 v2, 16, v3
	v_and_b32_e32 v3, 0xffff0000, v3
	v_add_f32_e32 v16, v22, v16
	v_pk_mul_f32 v[72:73], v[74:75], v[72:73]
	v_mul_f32_e32 v74, 0xbfb8aa3b, v2
	v_mul_f32_e32 v75, 0xbfb8aa3b, v3
	v_add_f32_e32 v16, v23, v16
	v_add_f32_e32 v70, 1.0, v70
	v_add_f32_e32 v71, 1.0, v71
	v_exp_f32_e32 v74, v74
	v_exp_f32_e32 v75, v75
	v_add_f32_e32 v8, v8, v16
	v_rcp_f32_e32 v70, v70
	v_rcp_f32_e32 v71, v71
	v_add_f32_e32 v8, v9, v8
	v_add_f32_e32 v8, v12, v8
	v_pk_mul_f32 v[10:11], v[14:15], v[14:15]
	s_waitcnt lgkmcnt(0)
	v_lshlrev_b32_e32 v14, 16, v4
	v_and_b32_e32 v15, 0xffff0000, v4
	v_add_f32_e32 v8, v13, v8
	v_pk_mul_f32 v[14:15], v[68:69], v[14:15]
	v_add_f32_e32 v74, 1.0, v74
	v_add_f32_e32 v75, 1.0, v75
	v_add_f32_e32 v8, v10, v8
	v_pk_mul_f32 v[68:69], v[14:15], v[14:15]
	v_lshlrev_b32_e32 v4, 16, v5
	v_and_b32_e32 v5, 0xffff0000, v5
	v_pk_mul_f32 v[0:1], v[70:71], v[0:1]
	v_rcp_f32_e32 v74, v74
	v_rcp_f32_e32 v75, v75
	v_add_f32_e32 v8, v11, v8
	v_pk_mul_f32 v[4:5], v[0:1], v[4:5]
	v_add_f32_e32 v8, v68, v8
	v_pk_mul_f32 v[0:1], v[4:5], v[4:5]
	v_lshlrev_b32_e32 v70, 16, v6
	v_and_b32_e32 v71, 0xffff0000, v6
	v_add_f32_e32 v8, v69, v8
	v_pk_mul_f32 v[70:71], v[72:73], v[70:71]
	v_add_f32_e32 v0, v0, v8
	v_pk_mul_f32 v[72:73], v[70:71], v[70:71]
	v_lshlrev_b32_e32 v6, 16, v7
	v_and_b32_e32 v7, 0xffff0000, v7
	v_pk_mul_f32 v[2:3], v[74:75], v[2:3]
	v_add_f32_e32 v0, v1, v0
	v_pk_mul_f32 v[6:7], v[2:3], v[6:7]
	v_add_f32_e32 v0, v72, v0
	v_pk_mul_f32 v[2:3], v[6:7], v[6:7]
	v_add_f32_e32 v0, v73, v0
	v_add_f32_e32 v0, v2, v0
	v_add_f32_e32 v8, v3, v0
	v_cvt_pk_bf16_f32 v0, v14, v15
	v_cvt_pk_bf16_f32 v1, v4, v5
	v_cvt_pk_bf16_f32 v2, v70, v71
	v_cvt_pk_bf16_f32 v3, v6, v7
	global_store_dwordx4 v[60:61], v[0:3], off offset:2160
	ds_write_b32 v156, v8
	s_waitcnt lgkmcnt(0)
	s_barrier
	s_and_saveexec_b64 vcc, s[66:67]
	s_cbranch_execz .LBB0_640
	ds_read2st64_b32 v[0:1], v140 offset1:1
	v_readlane_b32 s12, v253, 57
	v_readlane_b32 s13, v253, 58
	s_waitcnt lgkmcnt(0)
	v_add_f32_e32 v0, 0, v0
	v_add_f32_e32 v2, v0, v1
	ds_read2st64_b32 v[0:1], v140 offset0:2 offset1:3
	s_waitcnt lgkmcnt(0)
	v_add_f32_e32 v0, v2, v0
	v_add_f32_e32 v2, v0, v1
	ds_read2st64_b32 v[0:1], v140 offset0:4 offset1:5
	s_waitcnt lgkmcnt(0)
	v_add_f32_e32 v0, v2, v0
	v_add_f32_e32 v2, v0, v1
	ds_read2st64_b32 v[0:1], v140 offset0:6 offset1:7
	s_waitcnt lgkmcnt(0)
	v_add_f32_e32 v0, v2, v0
	v_add_f32_e32 v0, v0, v1
	v_fmamk_f32 v0, v0, 0x3b000000, v222
	v_rsq_f32_e32 v2, v0
	v_add_u32_e32 v0, s20, v133
	v_ashrrev_i32_e32 v1, 31, v0
	v_lshl_add_u64 v[0:1], v[0:1], 2, s[12:13]
	global_store_dword v[0:1], v2, off
	s_branch .LBB0_640
